# v41 stack + layer-0 gate/up GEMM unit-boundary hosting (1/8 of workgroups per boundary)
# speedup vs baseline: 1.0054x; 1.0023x over previous
; #define PG8_BAR __builtin_amdgcn_s_barrier()
; template <class Epi, class Sched, bool ALIGN_EPI = false, bool SP2 = false, bool F8 = false, bool BTILED = false, bool ATILED = false>
; __device__ __forceinline__ void gemm_phase(PG8_LAS unsigned char* lds, const Gemm g, const Sched& S, const Epi& E) {
;     ...
;         if constexpr (!Epi::AFTER_DRAIN) { E(acc, cur, wr, wc, fr, fq); S.done(cur); }
;         if (!has_next) break;
; #pragma unroll
;         for (int a = 0; a < 2; ++a)
; #pragma unroll
;             for (int b = 0; b < 2; ++b)
; #pragma unroll
;                 for (int m = 0; m < 4; ++m)
; #pragma unroll
;                     for (int n = 0; n < 2; ++n) acc[a][b][m][n] = (f32x4){0.f, 0.f, 0.f, 0.f};
;         cur = nxt; cA = nA; cB = nB; ++ui;
;         if constexpr (ALIGN_EPI) { if (wr == 1) PG8_BAR; }
;     }
.LBB0_1653:
	s_andn2_b64 vcc, exec, s[2:3]
	s_mov_b32 s43, s42
	s_mov_b32 s18, s10
	s_mov_b64 s[2:3], s[16:17]
	s_mov_b64 s[20:21], s[14:15]
	s_cbranch_vccz .LBB0_1663
	s_cmp_lg_u32 s54, 0
	s_cbranch_scc1 .Lh_skip
	s_add_u32 s100, s41, s88
	s_and_b32 s100, s100, 7
	s_cmp_lg_u32 s100, 0
	s_cbranch_scc1 .Lh_skip0
	v_writelane_b32 v222, s0, 0
	v_writelane_b32 v222, s1, 1
	v_writelane_b32 v222, s2, 2
	v_writelane_b32 v222, s3, 3
	v_writelane_b32 v222, s4, 4
	v_writelane_b32 v222, s5, 5
	v_writelane_b32 v222, s6, 6
	v_writelane_b32 v222, s7, 7
	v_writelane_b32 v222, s8, 8
	v_writelane_b32 v222, s9, 9
	v_writelane_b32 v222, s10, 10
	v_writelane_b32 v222, s11, 11
	v_writelane_b32 v222, s12, 12
	v_writelane_b32 v222, s13, 13
	v_writelane_b32 v222, s14, 14
	v_writelane_b32 v222, s15, 15
	v_writelane_b32 v222, s16, 16
	v_writelane_b32 v222, s17, 17
	v_writelane_b32 v222, s18, 18
	v_writelane_b32 v222, s19, 19
	v_writelane_b32 v222, s20, 20
	v_writelane_b32 v222, s21, 21
	v_writelane_b32 v222, s22, 22
	v_writelane_b32 v222, s23, 23
	v_writelane_b32 v222, s89, 24
	v_writelane_b32 v222, s94, 25
	v_mov_b32_e32 v223, v1
	v_mov_b32_e32 v221, v182
	s_mov_b32 s100, 0x1234
	s_branch .Lfl_entry
